# v12 + one-dword-per-lane L2 prefetch of the next unit's Q rows issued when the K/V prefetch cursor advances (MLA stream)
# speedup vs baseline: 1.0036x; 1.0036x over previous
.Lmla_f_adv:
	s_add_i32 s26, s54, 1
	s_bitcmp0_b32 s54, 0
	v_readlane_b32 s11, v252, 25
	s_mul_i32 s10, s26, s78
	s_cselect_b32 s20, s11, s82
	s_add_i32 s20, s20, s10
	s_cmpk_lt_i32 s20, 0x800
	s_cselect_b64 s[10:11], -1, 0
	s_cmpk_gt_i32 s20, 0x7ff
	s_cbranch_scc1 .LBB0_702
	s_lshl_b32 s1, s20, 5
	s_and_b32 s1, s1, 0xf00
	s_bfe_u32 s0, s20, 0x40007
	s_sub_i32 s1, 0x1000, s1
	s_lshl_b32 s28, s0, 12
	s_add_i32 s28, s28, s1
	s_addk_i32 s28, 0xff00
	v_add_u32_e32 v224, s28, v188
	s_and_b32 s29, s20, 7
	s_mul_i32 s29, s29, 0xc0
	v_lshl_add_u32 v225, v190, 3, s29
	s_movk_i32 s28, 0x600
	v_mad_u32_u24 v224, v224, s28, v225
	global_load_dword v230, v224, s[22:23]
	s_ashr_i32 s55, s1, 6
	s_mul_i32 s0, s0, 0x840000
	s_add_u32 s0, s62, s0
	s_addc_u32 s1, s63, 0
	s_lshl_b32 s14, s20, 8
	s_and_b32 s56, s14, 0x700
	s_add_u32 s14, s0, s56
	s_addc_u32 s15, s1, 0
	s_add_u32 s14, s14, 0x80
	s_addc_u32 s15, s15, 0

.Lmla_m_adv:
	s_add_i32 s26, s54, 1
	s_bitcmp0_b32 s54, 0
	v_readlane_b32 s21, v252, 25
	s_mul_i32 s20, s26, s78
	s_cselect_b32 s27, s21, s82
	s_add_i32 s27, s27, s20
	s_cmpk_lt_i32 s27, 0x800
	s_cselect_b64 s[20:21], -1, 0
	s_cmpk_gt_i32 s27, 0x7ff
	s_cbranch_scc1 .LBB0_751
	s_lshl_b32 s1, s27, 5
	s_and_b32 s1, s1, 0xf00
	s_bfe_u32 s0, s27, 0x40007
	s_sub_i32 s1, 0x1000, s1
	s_lshl_b32 s28, s0, 12
	s_add_i32 s28, s28, s1
	s_addk_i32 s28, 0xff00
	v_add_u32_e32 v224, s28, v188
	s_and_b32 s29, s27, 7
	s_mul_i32 s29, s29, 0xc0
	v_lshl_add_u32 v225, v190, 3, s29
	s_movk_i32 s28, 0x600
	v_mad_u32_u24 v224, v224, s28, v225
	global_load_dword v230, v224, s[22:23]
	s_ashr_i32 s55, s1, 6
	s_mul_i32 s0, s0, 0x840000
	s_add_u32 s0, s62, s0
	s_addc_u32 s1, s63, 0
	s_lshl_b32 s14, s27, 8
	s_and_b32 s56, s14, 0x700
	s_add_u32 s14, s0, s56
	s_addc_u32 s15, s1, 0
	s_add_u32 s14, s14, 0x80
	s_addc_u32 s15, s15, 0

.LBB0_775:
	s_andn2_b64 vcc, exec, s[28:29]
	s_cbranch_vccnz .LBB0_770
	s_add_i32 s26, s54, 1
	s_bitcmp0_b32 s54, 0
	v_readlane_b32 s11, v252, 25
	s_mul_i32 s10, s26, s78
	s_cselect_b32 s20, s11, s82
	s_add_i32 s20, s20, s10
	s_cmpk_lt_i32 s20, 0x800
	s_cselect_b64 s[10:11], -1, 0
	s_cmpk_gt_i32 s20, 0x7ff
	s_cbranch_scc1 .LBB0_778
	s_lshl_b32 s1, s20, 5
	s_and_b32 s1, s1, 0xf00
	s_bfe_u32 s0, s20, 0x40007
	s_sub_i32 s1, 0x1000, s1
	s_lshl_b32 s28, s0, 12
	s_add_i32 s28, s28, s1
	s_addk_i32 s28, 0xff00
	v_add_u32_e32 v224, s28, v188
	s_and_b32 s29, s20, 7
	s_mul_i32 s29, s29, 0xc0
	v_lshl_add_u32 v225, v190, 3, s29
	s_movk_i32 s28, 0x600
	v_mad_u32_u24 v224, v224, s28, v225
	global_load_dword v230, v224, s[22:23]
	s_ashr_i32 s55, s1, 6
	s_mul_i32 s0, s0, 0x840000
	s_add_u32 s0, s62, s0
	s_addc_u32 s1, s63, 0
	s_lshl_b32 s14, s20, 8
	s_and_b32 s56, s14, 0x700
	s_add_u32 s14, s0, s56
	s_addc_u32 s15, s1, 0
	s_add_u32 s14, s14, 0x80
	s_addc_u32 s15, s15, 0
